# opt22: opt4 + grid barrier: non-leader workgroups poll the global generation word instead of the per-XCD one; leaders' per-XCD generation increment removed (one memory round trip less per barrier)
# baseline (speedup 1.0000x reference)
.LBB0_111:
	s_or_b64 exec, exec, s[4:5]
	v_readlane_b32 s4, v252, 22
	v_readlane_b32 s5, v252, 23
	s_waitcnt vmcnt(0)
	buffer_inv sc1
	s_nop 2
	s_waitcnt vmcnt(0)

.LBB0_152:
	v_readlane_b32 s4, v252, 20
	v_readlane_b32 s5, v252, 21
	v_cvt_f32_u32_e32 v1, v2
	v_sub_u32_e32 v4, 0, v2
	v_rcp_iflag_f32_e32 v1, v1
	s_nop 1
	global_atomic_add v3, v97, v197, s[4:5] sc0
	v_mul_f32_e32 v1, 0x4f7ffffe, v1
	v_cvt_u32_f32_e32 v1, v1
	v_mul_lo_u32 v4, v4, v1
	v_mul_hi_u32 v4, v1, v4
	v_add_u32_e32 v1, v1, v4
	s_waitcnt vmcnt(0)
	v_mul_hi_u32 v1, v3, v1
	v_mul_lo_u32 v4, v1, v2
	v_sub_u32_e32 v4, v3, v4
	v_add_u32_e32 v5, 1, v1
	v_cmp_ge_u32_e32 vcc, v4, v2
	v_add_u32_e32 v3, 1, v3
	s_nop 0
	v_cndmask_b32_e32 v1, v1, v5, vcc
	v_sub_u32_e32 v5, v4, v2
	v_cndmask_b32_e32 v4, v4, v5, vcc
	v_add_u32_e32 v5, 1, v1
	v_cmp_ge_u32_e32 vcc, v4, v2
	s_nop 1
	v_cndmask_b32_e32 v1, v1, v5, vcc
	v_mul_lo_u32 v4, v2, v1
	v_add_u32_e32 v2, v4, v2
	v_cmp_ne_u32_e32 vcc, v3, v2
	s_and_saveexec_b64 s[4:5], vcc
	s_xor_b64 s[4:5], exec, s[4:5]
	s_cbranch_execz .LBB0_166
	v_readlane_b32 s6, v252, 26
	v_readlane_b32 s7, v252, 27
	s_waitcnt lgkmcnt(0)
	s_nop 3
	global_load_dword v0, v97, s[6:7] sc1
	s_waitcnt vmcnt(0)
	v_cmp_eq_u32_e32 vcc, v0, v1
	s_and_saveexec_b64 s[6:7], vcc
	s_cbranch_execz .LBB0_165
	s_mov_b32 s16, 1
	s_mov_b64 s[10:11], 0
	s_branch .LBB0_156

.LBB0_160:
	v_readlane_b32 s14, v252, 26
	v_readlane_b32 s15, v252, 27
	s_add_i32 s16, s16, 1
	s_mov_b64 s[18:19], -1
	s_nop 2
	global_load_dword v0, v97, s[14:15] sc1
	s_waitcnt vmcnt(0)
	v_cmp_ne_u32_e32 vcc, v0, v1
	s_orn2_b64 s[14:15], vcc, exec
	s_branch .LBB0_155

.LBB0_323:
	v_readlane_b32 s4, v252, 20
	v_readlane_b32 s5, v252, 21
	v_cvt_f32_u32_e32 v1, v2
	v_sub_u32_e32 v4, 0, v2
	v_rcp_iflag_f32_e32 v1, v1
	s_nop 1
	global_atomic_add v3, v97, v197, s[4:5] sc0
	v_mul_f32_e32 v1, 0x4f7ffffe, v1
	v_cvt_u32_f32_e32 v1, v1
	v_mul_lo_u32 v4, v4, v1
	v_mul_hi_u32 v4, v1, v4
	v_add_u32_e32 v1, v1, v4
	s_waitcnt vmcnt(0)
	v_mul_hi_u32 v1, v3, v1
	v_mul_lo_u32 v4, v1, v2
	v_sub_u32_e32 v4, v3, v4
	v_add_u32_e32 v5, 1, v1
	v_cmp_ge_u32_e32 vcc, v4, v2
	v_add_u32_e32 v3, 1, v3
	s_nop 0
	v_cndmask_b32_e32 v1, v1, v5, vcc
	v_sub_u32_e32 v5, v4, v2
	v_cndmask_b32_e32 v4, v4, v5, vcc
	v_add_u32_e32 v5, 1, v1
	v_cmp_ge_u32_e32 vcc, v4, v2
	s_nop 1
	v_cndmask_b32_e32 v1, v1, v5, vcc
	v_mul_lo_u32 v4, v2, v1
	v_add_u32_e32 v2, v4, v2
	v_cmp_ne_u32_e32 vcc, v3, v2
	s_and_saveexec_b64 s[4:5], vcc
	s_xor_b64 s[4:5], exec, s[4:5]
	s_cbranch_execz .LBB0_337
	v_readlane_b32 s6, v252, 26
	v_readlane_b32 s7, v252, 27
	s_waitcnt lgkmcnt(0)
	s_nop 3
	global_load_dword v0, v97, s[6:7] sc1
	s_waitcnt vmcnt(0)
	v_cmp_eq_u32_e32 vcc, v0, v1
	s_and_saveexec_b64 s[6:7], vcc
	s_cbranch_execz .LBB0_336
	s_mov_b32 s24, 1
	s_mov_b64 s[12:13], 0
	s_branch .LBB0_327

.LBB0_331:
	v_readlane_b32 s18, v252, 26
	v_readlane_b32 s19, v252, 27
	s_add_i32 s24, s24, 1
	s_mov_b64 s[20:21], -1
	s_nop 2
	global_load_dword v0, v97, s[18:19] sc1
	s_waitcnt vmcnt(0)
	v_cmp_ne_u32_e32 vcc, v0, v1
	s_orn2_b64 s[18:19], vcc, exec
	s_branch .LBB0_326

.LBB0_475:
	v_readlane_b32 s4, v252, 20
	v_readlane_b32 s5, v252, 21
	v_cvt_f32_u32_e32 v1, v2
	v_sub_u32_e32 v4, 0, v2
	v_rcp_iflag_f32_e32 v1, v1
	s_nop 1
	global_atomic_add v3, v97, v197, s[4:5] sc0
	v_mul_f32_e32 v1, 0x4f7ffffe, v1
	v_cvt_u32_f32_e32 v1, v1
	v_mul_lo_u32 v4, v4, v1
	v_mul_hi_u32 v4, v1, v4
	v_add_u32_e32 v1, v1, v4
	s_waitcnt vmcnt(0)
	v_mul_hi_u32 v1, v3, v1
	v_mul_lo_u32 v4, v1, v2
	v_sub_u32_e32 v4, v3, v4
	v_add_u32_e32 v5, 1, v1
	v_cmp_ge_u32_e32 vcc, v4, v2
	v_add_u32_e32 v3, 1, v3
	s_nop 0
	v_cndmask_b32_e32 v1, v1, v5, vcc
	v_sub_u32_e32 v5, v4, v2
	v_cndmask_b32_e32 v4, v4, v5, vcc
	v_add_u32_e32 v5, 1, v1
	v_cmp_ge_u32_e32 vcc, v4, v2
	s_nop 1
	v_cndmask_b32_e32 v1, v1, v5, vcc
	v_mul_lo_u32 v4, v2, v1
	v_add_u32_e32 v2, v4, v2
	v_cmp_ne_u32_e32 vcc, v3, v2
	s_and_saveexec_b64 s[4:5], vcc
	s_xor_b64 s[4:5], exec, s[4:5]
	s_cbranch_execz .LBB0_489
	v_readlane_b32 s6, v252, 26
	v_readlane_b32 s7, v252, 27
	s_waitcnt lgkmcnt(0)
	s_nop 3
	global_load_dword v0, v97, s[6:7] sc1
	s_waitcnt vmcnt(0)
	v_cmp_eq_u32_e32 vcc, v0, v1
	s_and_saveexec_b64 s[6:7], vcc
	s_cbranch_execz .LBB0_488
	s_mov_b32 s16, 1
	s_mov_b64 s[12:13], 0
	s_branch .LBB0_479

.LBB0_483:
	v_readlane_b32 s18, v252, 26
	v_readlane_b32 s19, v252, 27
	s_add_i32 s16, s16, 1
	s_mov_b64 s[20:21], -1
	s_nop 2
	global_load_dword v0, v97, s[18:19] sc1
	s_waitcnt vmcnt(0)
	v_cmp_ne_u32_e32 vcc, v0, v1
	s_orn2_b64 s[18:19], vcc, exec
	s_branch .LBB0_478

.LBB0_1193:
	v_readlane_b32 s4, v252, 20
	v_readlane_b32 s5, v252, 21
	v_cvt_f32_u32_e32 v1, v2
	v_sub_u32_e32 v4, 0, v2
	v_rcp_iflag_f32_e32 v1, v1
	s_nop 1
	global_atomic_add v3, v97, v197, s[4:5] sc0
	v_mul_f32_e32 v1, 0x4f7ffffe, v1
	v_cvt_u32_f32_e32 v1, v1
	v_mul_lo_u32 v4, v4, v1
	v_mul_hi_u32 v4, v1, v4
	v_add_u32_e32 v1, v1, v4
	s_waitcnt vmcnt(0)
	v_mul_hi_u32 v1, v3, v1
	v_mul_lo_u32 v4, v1, v2
	v_sub_u32_e32 v4, v3, v4
	v_add_u32_e32 v5, 1, v1
	v_cmp_ge_u32_e32 vcc, v4, v2
	v_add_u32_e32 v3, 1, v3
	s_nop 0
	v_cndmask_b32_e32 v1, v1, v5, vcc
	v_sub_u32_e32 v5, v4, v2
	v_cndmask_b32_e32 v4, v4, v5, vcc
	v_add_u32_e32 v5, 1, v1
	v_cmp_ge_u32_e32 vcc, v4, v2
	s_nop 1
	v_cndmask_b32_e32 v1, v1, v5, vcc
	v_mul_lo_u32 v4, v2, v1
	v_add_u32_e32 v2, v4, v2
	v_cmp_ne_u32_e32 vcc, v3, v2
	s_and_saveexec_b64 s[4:5], vcc
	s_xor_b64 s[4:5], exec, s[4:5]
	s_cbranch_execz .LBB0_1207
	v_readlane_b32 s6, v252, 26
	v_readlane_b32 s7, v252, 27
	s_waitcnt lgkmcnt(0)
	s_nop 3
	global_load_dword v0, v97, s[6:7] sc1
	s_waitcnt vmcnt(0)
	v_cmp_eq_u32_e32 vcc, v0, v1
	s_and_saveexec_b64 s[6:7], vcc
	s_cbranch_execz .LBB0_1206
	s_mov_b32 s20, 1
	s_mov_b64 s[8:9], 0
	s_branch .LBB0_1197

.LBB0_1201:
	v_readlane_b32 s12, v252, 26
	v_readlane_b32 s13, v252, 27
	s_add_i32 s20, s20, 1
	s_mov_b64 s[14:15], -1
	s_nop 2
	global_load_dword v0, v97, s[12:13] sc1
	s_waitcnt vmcnt(0)
	v_cmp_ne_u32_e32 vcc, v0, v1
	s_orn2_b64 s[12:13], vcc, exec
	s_branch .LBB0_1196

.LBB0_1479:
	v_readlane_b32 s4, v252, 20
	v_readlane_b32 s5, v252, 21
	v_cvt_f32_u32_e32 v1, v2
	v_sub_u32_e32 v4, 0, v2
	v_rcp_iflag_f32_e32 v1, v1
	s_nop 1
	global_atomic_add v3, v97, v197, s[4:5] sc0
	v_mul_f32_e32 v1, 0x4f7ffffe, v1
	v_cvt_u32_f32_e32 v1, v1
	v_mul_lo_u32 v4, v4, v1
	v_mul_hi_u32 v4, v1, v4
	v_add_u32_e32 v1, v1, v4
	s_waitcnt vmcnt(0)
	v_mul_hi_u32 v1, v3, v1
	v_mul_lo_u32 v4, v1, v2
	v_sub_u32_e32 v4, v3, v4
	v_add_u32_e32 v5, 1, v1
	v_cmp_ge_u32_e32 vcc, v4, v2
	v_add_u32_e32 v3, 1, v3
	s_nop 0
	v_cndmask_b32_e32 v1, v1, v5, vcc
	v_sub_u32_e32 v5, v4, v2
	v_cndmask_b32_e32 v4, v4, v5, vcc
	v_add_u32_e32 v5, 1, v1
	v_cmp_ge_u32_e32 vcc, v4, v2
	s_nop 1
	v_cndmask_b32_e32 v1, v1, v5, vcc
	v_mul_lo_u32 v4, v2, v1
	v_add_u32_e32 v2, v4, v2
	v_cmp_ne_u32_e32 vcc, v3, v2
	s_and_saveexec_b64 s[4:5], vcc
	s_xor_b64 s[4:5], exec, s[4:5]
	s_cbranch_execz .LBB0_1493
	v_readlane_b32 s6, v252, 26
	v_readlane_b32 s7, v252, 27
	s_waitcnt lgkmcnt(0)
	s_nop 3
	global_load_dword v0, v97, s[6:7] sc1
	s_waitcnt vmcnt(0)
	v_cmp_eq_u32_e32 vcc, v0, v1
	s_and_saveexec_b64 s[6:7], vcc
	s_cbranch_execz .LBB0_1492
	s_mov_b32 s16, 1
	s_mov_b64 s[8:9], 0
	s_branch .LBB0_1483

.LBB0_1487:
	v_readlane_b32 s12, v252, 26
	v_readlane_b32 s13, v252, 27
	s_add_i32 s16, s16, 1
	s_mov_b64 s[14:15], -1
	s_nop 2
	global_load_dword v0, v97, s[12:13] sc1
	s_waitcnt vmcnt(0)
	v_cmp_ne_u32_e32 vcc, v0, v1
	s_orn2_b64 s[12:13], vcc, exec
	s_branch .LBB0_1482
